# LayerNorm1 token loop: next iteration's first row prefetched behind the second row's loads; gain/bias quads hoisted out of the token loop into unused registers
# speedup vs baseline: 1.0154x; 1.0008x over previous
.LBB0_704:
	s_or_b64 exec, exec, s[12:13]
	s_mov_b32 s36, -2
	v_mov_b64_e32 v[2:3], v[46:47]
	v_mov_b64_e32 v[4:5], v[44:45]
	s_mov_b32 s37, s40
	s_mov_b64 s[14:15], s[20:21]
	ds_read_b128 v[180:183], v132
	ds_read_b128 v[184:187], v132 offset:8192
	ds_read_b128 v[188:191], v132 offset:1024
	ds_read_b128 v[192:195], v132 offset:9216
	ds_read_b128 v[196:199], v132 offset:2048
	ds_read_b128 v[200:203], v132 offset:10240
	ds_read_b128 v[204:207], v132 offset:3072
	ds_read_b128 v[208:211], v132 offset:11264
	ds_read_b128 v[212:215], v132 offset:4096
	ds_read_b128 v[216:219], v132 offset:12288
	ds_read_b128 v[220:223], v132 offset:5120
	ds_read_b128 v[224:227], v132 offset:13312
	ds_read_b128 v[228:231], v132 offset:6144
	ds_read_b128 v[232:235], v132 offset:14336
	ds_read_b128 v[236:239], v132 offset:7168
	ds_read_b128 v[240:243], v132 offset:15360
	v_lshl_add_u64 v[176:177], s[92:93], 0, v[4:5]
	s_mov_b32 s12, 0x69400000
	s_mov_b32 s13, 0
	v_lshl_add_u64 v[176:177], v[176:177], 0, s[12:13]
	global_load_dwordx2 v[160:161], v[176:177], off
	global_load_dwordx2 v[162:163], v[176:177], off offset:512
	global_load_dwordx2 v[164:165], v[176:177], off offset:1024
	global_load_dwordx2 v[166:167], v[176:177], off offset:1536
	global_load_dwordx2 v[168:169], v[176:177], off offset:2048
	global_load_dwordx2 v[170:171], v[176:177], off offset:2560
	global_load_dwordx2 v[172:173], v[176:177], off offset:3072
	global_load_dwordx2 v[174:175], v[176:177], off offset:3584
	s_waitcnt vmcnt(0)
	s_waitcnt lgkmcnt(0)
	s_branch .LBB0_706

.LBB0_706:
	v_lshl_add_u64 v[8:9], s[92:93], 0, v[4:5]
	v_add_co_u32_e32 v10, vcc, 0x69400000, v8
	v_mov_b32_e32 v144, 0
	s_nop 0
	v_addc_co_u32_e32 v11, vcc, 0, v9, vcc
	v_add_co_u32_e32 v8, vcc, s43, v8
	v_lshl_add_u32 v144, v144, 2, v132
	s_nop 0
	v_addc_co_u32_e32 v9, vcc, 0, v9, vcc
	s_waitcnt vmcnt(16)
	v_lshlrev_b32_e32 v6, 16, v160
	v_and_b32_e32 v7, 0xffff0000, v160
	v_lshlrev_b32_e32 v70, 16, v161
	v_and_b32_e32 v71, 0xffff0000, v161
	v_add_f32_e32 v12, v6, v7
	v_add_f32_e32 v13, v70, v71
	v_add_f32_e32 v12, v12, v13
	v_add_f32_e32 v14, 0, v12
	v_lshlrev_b32_e32 v66, 16, v162
	v_and_b32_e32 v67, 0xffff0000, v162
	v_lshlrev_b32_e32 v68, 16, v163
	v_and_b32_e32 v69, 0xffff0000, v163
	v_add_f32_e32 v12, v66, v67
	v_add_f32_e32 v13, v68, v69
	v_add_f32_e32 v12, v12, v13
	v_add_f32_e32 v14, v14, v12
	v_lshlrev_b32_e32 v64, 16, v164
	v_and_b32_e32 v65, 0xffff0000, v164
	v_lshlrev_b32_e32 v62, 16, v165
	v_and_b32_e32 v63, 0xffff0000, v165
	v_add_f32_e32 v12, v64, v65
	v_add_f32_e32 v13, v62, v63
	v_add_f32_e32 v12, v12, v13
	v_add_f32_e32 v14, v14, v12
	v_lshlrev_b32_e32 v58, 16, v166
	v_and_b32_e32 v59, 0xffff0000, v166
	v_lshlrev_b32_e32 v60, 16, v167
	v_and_b32_e32 v61, 0xffff0000, v167
	v_add_f32_e32 v12, v58, v59
	v_add_f32_e32 v13, v60, v61
	v_add_f32_e32 v12, v12, v13
	v_add_f32_e32 v14, v14, v12
	v_lshlrev_b32_e32 v56, 16, v168
	v_and_b32_e32 v57, 0xffff0000, v168
	v_lshlrev_b32_e32 v54, 16, v169
	v_and_b32_e32 v55, 0xffff0000, v169
	v_add_f32_e32 v12, v56, v57
	v_add_f32_e32 v13, v54, v55
	v_add_f32_e32 v12, v12, v13
	v_add_f32_e32 v14, v14, v12
	v_lshlrev_b32_e32 v32, 16, v170
	v_and_b32_e32 v33, 0xffff0000, v170
	v_lshlrev_b32_e32 v52, 16, v171
	v_and_b32_e32 v53, 0xffff0000, v171
	v_add_f32_e32 v12, v32, v33
	v_add_f32_e32 v13, v52, v53
	v_add_f32_e32 v12, v12, v13
	v_add_f32_e32 v14, v14, v12
	v_lshlrev_b32_e32 v30, 16, v172
	v_and_b32_e32 v31, 0xffff0000, v172
	v_lshlrev_b32_e32 v28, 16, v173
	v_and_b32_e32 v29, 0xffff0000, v173
	v_add_f32_e32 v12, v30, v31
	v_add_f32_e32 v13, v28, v29
	v_add_f32_e32 v12, v12, v13
	v_add_f32_e32 v12, v14, v12
	v_lshlrev_b32_e32 v24, 16, v174
	v_and_b32_e32 v25, 0xffff0000, v174
	v_lshlrev_b32_e32 v26, 16, v175
	v_and_b32_e32 v27, 0xffff0000, v175
	v_add_f32_e32 v10, v24, v25
	v_add_f32_e32 v11, v26, v27
	v_add_f32_e32 v10, v10, v11
	v_add_f32_e32 v34, v12, v10
	global_load_dwordx2 v[22:23], v[8:9], off
	global_load_dwordx2 v[20:21], v[8:9], off offset:512
	global_load_dwordx2 v[18:19], v[8:9], off offset:1024
	global_load_dwordx2 v[16:17], v[8:9], off offset:1536
	global_load_dwordx2 v[14:15], v[8:9], off offset:2048
	global_load_dwordx2 v[12:13], v[8:9], off offset:2560
	global_load_dwordx2 v[10:11], v[8:9], off offset:3072
	s_nop 0
	global_load_dwordx2 v[8:9], v[8:9], off offset:3584
	s_cmp_lt_i32 s36, 4
	s_cselect_b32 s12, s30, 0
	s_cselect_b32 s13, s31, 0
	v_lshl_add_u64 v[176:177], v[4:5], 0, s[12:13]
	v_lshl_add_u64 v[176:177], s[92:93], 0, v[176:177]
	s_mov_b32 s12, 0x69400000
	s_mov_b32 s13, 0
	v_lshl_add_u64 v[176:177], v[176:177], 0, s[12:13]
	global_load_dwordx2 v[160:161], v[176:177], off
	global_load_dwordx2 v[162:163], v[176:177], off offset:512
	global_load_dwordx2 v[164:165], v[176:177], off offset:1024
	global_load_dwordx2 v[166:167], v[176:177], off offset:1536
	global_load_dwordx2 v[168:169], v[176:177], off offset:2048
	global_load_dwordx2 v[170:171], v[176:177], off offset:2560
	global_load_dwordx2 v[172:173], v[176:177], off offset:3072
	global_load_dwordx2 v[174:175], v[176:177], off offset:3584
	v_add_f32_dpp v34, v34, v34 quad_perm:[1,0,3,2] row_mask:0xf bank_mask:0xf bound_ctrl:1
	s_nop 1
	v_add_f32_dpp v34, v34, v34 quad_perm:[2,3,0,1] row_mask:0xf bank_mask:0xf bound_ctrl:1
	s_nop 1
	v_add_f32_dpp v34, v34, v34 row_half_mirror row_mask:0xf bank_mask:0xf bound_ctrl:1
	s_nop 1
	v_add_f32_dpp v34, v34, v34 row_mirror row_mask:0xf bank_mask:0xf bound_ctrl:1
	v_mov_b32_e32 v145, v34
	s_nop 1
	v_permlane16_swap_b32_e32 v34, v145
	v_add_f32_e32 v34, v34, v145
	v_mov_b32_e32 v145, v34
	s_nop 1
	v_permlane32_swap_b32_e32 v34, v145
	v_add_f32_e32 v145, v34, v145
	v_fmac_f32_e32 v71, 0xba000000, v145
	v_fmac_f32_e32 v7, 0xba000000, v145
	v_fmac_f32_e32 v70, 0xba000000, v145
	v_fmac_f32_e32 v6, 0xba000000, v145
	v_mul_f32_e32 v34, v7, v7
	v_mul_f32_e32 v146, v71, v71
	v_fmac_f32_e32 v34, v6, v6
	v_fmac_f32_e32 v146, v70, v70
	v_fmac_f32_e32 v69, 0xba000000, v145
	v_fmac_f32_e32 v67, 0xba000000, v145
	v_add_f32_e32 v34, v34, v146
	v_fmac_f32_e32 v68, 0xba000000, v145
	v_fmac_f32_e32 v66, 0xba000000, v145
	v_mul_f32_e32 v146, v67, v67
	v_mul_f32_e32 v147, v69, v69
	v_fmac_f32_e32 v146, v66, v66
	v_fmac_f32_e32 v147, v68, v68
	v_add_f32_e32 v146, v146, v147
	v_fmac_f32_e32 v63, 0xba000000, v145
	v_fmac_f32_e32 v65, 0xba000000, v145
	v_add_f32_e32 v34, v34, v146
	v_fmac_f32_e32 v62, 0xba000000, v145
	v_fmac_f32_e32 v64, 0xba000000, v145
	v_mul_f32_e32 v146, v65, v65
	v_mul_f32_e32 v147, v63, v63
	v_fmac_f32_e32 v146, v64, v64
	v_fmac_f32_e32 v147, v62, v62
	v_add_f32_e32 v146, v146, v147
	v_fmac_f32_e32 v61, 0xba000000, v145
	v_fmac_f32_e32 v59, 0xba000000, v145
	v_add_f32_e32 v34, v146, v34
	v_fmac_f32_e32 v60, 0xba000000, v145
	v_fmac_f32_e32 v58, 0xba000000, v145
	v_mul_f32_e32 v146, v59, v59
	v_mul_f32_e32 v147, v61, v61
	v_fmac_f32_e32 v146, v58, v58
	v_fmac_f32_e32 v147, v60, v60
	v_add_f32_e32 v146, v146, v147
	v_fmac_f32_e32 v55, 0xba000000, v145
	v_fmac_f32_e32 v57, 0xba000000, v145
	v_add_f32_e32 v34, v146, v34
	v_fmac_f32_e32 v54, 0xba000000, v145
	v_fmac_f32_e32 v56, 0xba000000, v145
	v_mul_f32_e32 v146, v57, v57
	v_mul_f32_e32 v147, v55, v55
	v_fmac_f32_e32 v146, v56, v56
	v_fmac_f32_e32 v147, v54, v54
	v_add_f32_e32 v146, v146, v147
	v_fmac_f32_e32 v53, 0xba000000, v145
	v_fmac_f32_e32 v33, 0xba000000, v145
	v_add_f32_e32 v34, v146, v34
	v_fmac_f32_e32 v52, 0xba000000, v145
	v_fmac_f32_e32 v32, 0xba000000, v145
	v_mul_f32_e32 v146, v33, v33
	v_mul_f32_e32 v147, v53, v53
	v_fmac_f32_e32 v146, v32, v32
	v_fmac_f32_e32 v147, v52, v52
	v_add_f32_e32 v146, v146, v147
	v_fmac_f32_e32 v29, 0xba000000, v145
	v_fmac_f32_e32 v31, 0xba000000, v145
	v_add_f32_e32 v34, v146, v34
	v_fmac_f32_e32 v28, 0xba000000, v145
	v_fmac_f32_e32 v30, 0xba000000, v145
	v_mul_f32_e32 v146, v31, v31
	v_mul_f32_e32 v147, v29, v29
	v_fmac_f32_e32 v146, v30, v30
	v_fmac_f32_e32 v147, v28, v28
	v_add_f32_e32 v146, v146, v147
	v_fmac_f32_e32 v27, 0xba000000, v145
	v_fmac_f32_e32 v25, 0xba000000, v145
	v_add_f32_e32 v34, v146, v34
	v_fmac_f32_e32 v26, 0xba000000, v145
	v_fmac_f32_e32 v24, 0xba000000, v145
	v_mul_f32_e32 v146, v25, v25
	v_mul_f32_e32 v147, v27, v27
	v_fmac_f32_e32 v146, v24, v24
	v_fmac_f32_e32 v147, v26, v26
	v_add_f32_e32 v146, v146, v147
	v_add_f32_e32 v34, v146, v34
	s_nop 1
	v_add_f32_dpp v34, v34, v34 quad_perm:[1,0,3,2] row_mask:0xf bank_mask:0xf bound_ctrl:1
	s_nop 1
	v_add_f32_dpp v34, v34, v34 quad_perm:[2,3,0,1] row_mask:0xf bank_mask:0xf bound_ctrl:1
	s_nop 1
	v_add_f32_dpp v34, v34, v34 row_half_mirror row_mask:0xf bank_mask:0xf bound_ctrl:1
	s_nop 1
	v_add_f32_dpp v34, v34, v34 row_mirror row_mask:0xf bank_mask:0xf bound_ctrl:1
	v_mov_b32_e32 v146, v34
	s_nop 1
	v_permlane16_swap_b32_e32 v34, v146
	v_add_f32_e32 v34, v34, v146
	v_mov_b32_e32 v146, v34
	s_nop 1
	v_permlane32_swap_b32_e32 v34, v146
	v_add_f32_e32 v34, v34, v146
	v_fmamk_f32 v34, v34, 0x3a000000, v135
	v_cmp_gt_f32_e32 vcc, s44, v34
	v_mul_f32_e32 v146, 0x4f800000, v34
	s_nop 0
	v_cndmask_b32_e32 v34, v34, v146, vcc
	v_sqrt_f32_e32 v146, v34
	s_nop 0
	v_add_u32_e32 v147, -1, v146
	v_fma_f32 v148, -v147, v146, v34
	v_cmp_ge_f32_e64 s[12:13], 0, v148
	v_add_u32_e32 v148, 1, v146
	s_nop 0
	v_cndmask_b32_e64 v147, v146, v147, s[12:13]
	v_fma_f32 v146, -v148, v146, v34
	v_cmp_lt_f32_e64 s[12:13], 0, v146
	s_nop 1
	v_cndmask_b32_e64 v146, v147, v148, s[12:13]
	v_mul_f32_e32 v147, 0x37800000, v146
	v_cndmask_b32_e32 v146, v146, v147, vcc
	v_cmp_class_f32_e32 vcc, v34, v136
	s_nop 1
	v_cndmask_b32_e32 v34, v146, v34, vcc
	v_div_scale_f32 v146, s[12:13], v34, v34, 1.0
	v_rcp_f32_e32 v147, v146
	s_nop 0
	v_fma_f32 v148, -v146, v147, 1.0
	v_fmac_f32_e32 v147, v148, v147
	v_div_scale_f32 v148, vcc, 1.0, v34, 1.0
	v_mul_f32_e32 v149, v148, v147
	v_fma_f32 v150, -v146, v149, v148
	v_fmac_f32_e32 v149, v150, v147
	v_fma_f32 v146, -v146, v149, v148
	v_div_fmas_f32 v146, v146, v147, v149
	v_div_fixup_f32 v34, v146, v34, 1.0
	v_pk_mul_f32 v[6:7], v[6:7], v[34:35] op_sel_hi:[1,0]
	v_pk_mul_f32 v[70:71], v[70:71], v[34:35] op_sel_hi:[1,0]
	v_pk_mul_f32 v[66:67], v[66:67], v[34:35] op_sel_hi:[1,0]
	v_pk_mul_f32 v[68:69], v[68:69], v[34:35] op_sel_hi:[1,0]
	v_pk_fma_f32 v[6:7], v[180:181], v[6:7], v[184:185]
	v_cvt_pk_fp8_f32 v146, v6, v7
	v_pk_fma_f32 v[70:71], v[182:183], v[70:71], v[186:187]
	v_lshl_add_u64 v[6:7], s[92:93], 0, v[2:3]
	v_pk_mul_f32 v[64:65], v[64:65], v[34:35] op_sel_hi:[1,0]
	v_cvt_pk_fp8_f32 v146, v70, v71 op_sel:[0,0,1]
	v_pk_mul_f32 v[62:63], v[62:63], v[34:35] op_sel_hi:[1,0]
	v_pk_mul_f32 v[58:59], v[58:59], v[34:35] op_sel_hi:[1,0]
	global_store_dword v[6:7], v146, off offset:-2048
	v_pk_mul_f32 v[60:61], v[60:61], v[34:35] op_sel_hi:[1,0]
	v_pk_mul_f32 v[56:57], v[56:57], v[34:35] op_sel_hi:[1,0]
	v_pk_mul_f32 v[54:55], v[54:55], v[34:35] op_sel_hi:[1,0]
	v_pk_mul_f32 v[32:33], v[32:33], v[34:35] op_sel_hi:[1,0]
	v_pk_fma_f32 v[66:67], v[188:189], v[66:67], v[192:193]
	v_pk_fma_f32 v[68:69], v[190:191], v[68:69], v[194:195]
	v_cvt_pk_fp8_f32 v70, v66, v67
	v_pk_mul_f32 v[52:53], v[52:53], v[34:35] op_sel_hi:[1,0]
	v_pk_mul_f32 v[30:31], v[30:31], v[34:35] op_sel_hi:[1,0]
	v_pk_mul_f32 v[28:29], v[28:29], v[34:35] op_sel_hi:[1,0]
	v_cvt_pk_fp8_f32 v70, v68, v69 op_sel:[0,0,1]
	v_pk_mul_f32 v[24:25], v[24:25], v[34:35] op_sel_hi:[1,0]
	v_pk_mul_f32 v[26:27], v[26:27], v[34:35] op_sel_hi:[1,0]
	global_store_dword v[6:7], v70, off offset:-1792
	v_pk_fma_f32 v[64:65], v[64:65], v[196:197], v[200:201]
	v_cvt_pk_fp8_f32 v66, v64, v65
	v_pk_fma_f32 v[62:63], v[62:63], v[198:199], v[202:203]
	s_nop 0
	v_cvt_pk_fp8_f32 v66, v62, v63 op_sel:[0,0,1]
	global_store_dword v[6:7], v66, off offset:-1536
	v_pk_fma_f32 v[58:59], v[58:59], v[204:205], v[208:209]
	v_cvt_pk_fp8_f32 v62, v58, v59
	v_pk_fma_f32 v[60:61], v[60:61], v[206:207], v[210:211]
	s_nop 0
	v_cvt_pk_fp8_f32 v62, v60, v61 op_sel:[0,0,1]
	global_store_dword v[6:7], v62, off offset:-1280
	v_pk_fma_f32 v[56:57], v[56:57], v[212:213], v[216:217]
	v_cvt_pk_fp8_f32 v58, v56, v57
	v_pk_fma_f32 v[54:55], v[54:55], v[214:215], v[218:219]
	s_nop 0
	v_cvt_pk_fp8_f32 v58, v54, v55 op_sel:[0,0,1]
	global_store_dword v[6:7], v58, off offset:-1024
	v_pk_fma_f32 v[32:33], v[32:33], v[220:221], v[224:225]
	v_cvt_pk_fp8_f32 v54, v32, v33
	v_pk_fma_f32 v[52:53], v[52:53], v[222:223], v[226:227]
	v_cvt_pk_fp8_f32 v54, v52, v53 op_sel:[0,0,1]
	global_store_dword v[6:7], v54, off offset:-768
	v_pk_fma_f32 v[30:31], v[30:31], v[228:229], v[232:233]
	s_nop 0
	v_cvt_pk_fp8_f32 v32, v30, v31
	v_pk_fma_f32 v[28:29], v[28:29], v[230:231], v[234:235]
	s_nop 0
	v_cvt_pk_fp8_f32 v32, v28, v29 op_sel:[0,0,1]
	global_store_dword v[6:7], v32, off offset:-512
	v_pk_fma_f32 v[24:25], v[24:25], v[236:237], v[240:241]
	v_cvt_pk_fp8_f32 v28, v24, v25
	v_pk_fma_f32 v[26:27], v[26:27], v[238:239], v[242:243]
	s_nop 0
	v_cvt_pk_fp8_f32 v28, v26, v27 op_sel:[0,0,1]
	global_store_dword v[6:7], v28, off offset:-256
	s_and_saveexec_b64 s[12:13], s[8:9]
	s_cbranch_execz .LBB0_708
	s_add_i32 s70, s37, -8
	s_add_u32 s68, s92, s14
	v_mul_f32_e32 v24, 0x3a000000, v145
	s_addc_u32 s69, s93, s15
	v_mov_b32_e32 v25, v34
	v_mov_b32_e32 v26, s70
	ds_write_b64 v26, v[24:25]
	global_store_dwordx2 v137, v[24:25], s[68:69]
.LBB0_708:
	s_or_b64 exec, exec, s[12:13]
	s_waitcnt vmcnt(23)
	v_lshlrev_b32_e32 v58, 16, v22
	v_and_b32_e32 v59, 0xffff0000, v22
	v_lshlrev_b32_e32 v56, 16, v23
	v_and_b32_e32 v57, 0xffff0000, v23
	v_add_f32_e32 v22, v58, v59
	v_add_f32_e32 v23, v56, v57
	s_waitcnt vmcnt(22)
	v_lshlrev_b32_e32 v52, 16, v20
	v_and_b32_e32 v53, 0xffff0000, v20
	v_lshlrev_b32_e32 v54, 16, v21
	v_and_b32_e32 v55, 0xffff0000, v21
	v_add_f32_e32 v22, v22, v23
	v_add_f32_e32 v20, v52, v53
	v_add_f32_e32 v21, v54, v55
	s_waitcnt vmcnt(21)
	v_lshlrev_b32_e32 v32, 16, v18
	v_and_b32_e32 v33, 0xffff0000, v18
	v_lshlrev_b32_e32 v30, 16, v19
	v_and_b32_e32 v31, 0xffff0000, v19
	v_add_f32_e32 v22, 0, v22
	v_add_f32_e32 v20, v20, v21
	v_add_f32_e32 v18, v32, v33
	v_add_f32_e32 v19, v30, v31
	v_add_f32_e32 v20, v22, v20
	v_add_f32_e32 v18, v18, v19
	s_waitcnt vmcnt(20)
	v_lshlrev_b32_e32 v26, 16, v16
	v_and_b32_e32 v27, 0xffff0000, v16
	v_lshlrev_b32_e32 v28, 16, v17
	v_and_b32_e32 v29, 0xffff0000, v17
	v_add_f32_e32 v18, v20, v18
	v_add_f32_e32 v16, v26, v27
	v_add_f32_e32 v17, v28, v29
	s_waitcnt vmcnt(19)
	v_lshlrev_b32_e32 v22, 16, v14
	v_and_b32_e32 v23, 0xffff0000, v14
	v_lshlrev_b32_e32 v20, 16, v15
	v_and_b32_e32 v21, 0xffff0000, v15
	v_add_f32_e32 v16, v16, v17
	v_add_f32_e32 v14, v22, v23
	v_add_f32_e32 v15, v20, v21
	v_add_f32_e32 v16, v18, v16
	v_add_f32_e32 v14, v14, v15
	v_add_f32_e32 v14, v16, v14
	s_waitcnt vmcnt(18)
	v_lshlrev_b32_e32 v16, 16, v12
	v_and_b32_e32 v17, 0xffff0000, v12
	v_lshlrev_b32_e32 v18, 16, v13
	v_and_b32_e32 v19, 0xffff0000, v13
	v_add_f32_e32 v12, v16, v17
	v_add_f32_e32 v13, v18, v19
	v_add_f32_e32 v12, v12, v13
	v_add_f32_e32 v24, v14, v12
	s_waitcnt vmcnt(17)
	v_lshlrev_b32_e32 v14, 16, v10
	v_and_b32_e32 v15, 0xffff0000, v10
	v_lshlrev_b32_e32 v12, 16, v11
	v_and_b32_e32 v13, 0xffff0000, v11
	v_add_f32_e32 v10, v14, v15
	v_add_f32_e32 v11, v12, v13
	v_add_f32_e32 v10, v10, v11
	v_add_f32_e32 v24, v24, v10
	s_waitcnt vmcnt(16)
	v_lshlrev_b32_e32 v10, 16, v8
	v_and_b32_e32 v11, 0xffff0000, v8
	v_lshlrev_b32_e32 v8, 16, v9
	v_and_b32_e32 v9, 0xffff0000, v9
	v_add_f32_e32 v25, v10, v11
	v_add_f32_e32 v34, v8, v9
	v_add_f32_e32 v25, v25, v34
	v_add_f32_e32 v24, v24, v25
	s_nop 1
	v_add_f32_dpp v24, v24, v24 quad_perm:[1,0,3,2] row_mask:0xf bank_mask:0xf bound_ctrl:1
	s_nop 1
	v_add_f32_dpp v24, v24, v24 quad_perm:[2,3,0,1] row_mask:0xf bank_mask:0xf bound_ctrl:1
	s_nop 1
	v_add_f32_dpp v24, v24, v24 row_half_mirror row_mask:0xf bank_mask:0xf bound_ctrl:1
	s_nop 1
	v_add_f32_dpp v24, v24, v24 row_mirror row_mask:0xf bank_mask:0xf bound_ctrl:1
	v_mov_b32_e32 v25, v24
	s_nop 1
	v_permlane16_swap_b32_e32 v24, v25
	v_add_f32_e32 v24, v24, v25
	v_mov_b32_e32 v25, v24
	s_nop 1
	v_permlane32_swap_b32_e32 v24, v25
	v_add_f32_e32 v25, v24, v25
	v_fmac_f32_e32 v57, 0xba000000, v25
	v_fmac_f32_e32 v59, 0xba000000, v25
	v_fmac_f32_e32 v56, 0xba000000, v25
	v_fmac_f32_e32 v58, 0xba000000, v25
	v_mul_f32_e32 v24, v59, v59
	v_mul_f32_e32 v34, v57, v57
	v_fmac_f32_e32 v24, v58, v58
	v_fmac_f32_e32 v34, v56, v56
	v_fmac_f32_e32 v55, 0xba000000, v25
	v_fmac_f32_e32 v53, 0xba000000, v25
	v_add_f32_e32 v24, v24, v34
	v_fmac_f32_e32 v54, 0xba000000, v25
	v_fmac_f32_e32 v52, 0xba000000, v25
	v_mul_f32_e32 v34, v53, v53
	v_mul_f32_e32 v60, v55, v55
	v_fmac_f32_e32 v34, v52, v52
	v_fmac_f32_e32 v60, v54, v54
	v_add_f32_e32 v34, v34, v60
	v_fmac_f32_e32 v31, 0xba000000, v25
	v_fmac_f32_e32 v33, 0xba000000, v25
	v_add_f32_e32 v24, v24, v34
	v_fmac_f32_e32 v30, 0xba000000, v25
	v_fmac_f32_e32 v32, 0xba000000, v25
	v_mul_f32_e32 v34, v33, v33
	v_mul_f32_e32 v60, v31, v31
	v_fmac_f32_e32 v34, v32, v32
	v_fmac_f32_e32 v60, v30, v30
	v_add_f32_e32 v34, v34, v60
	v_fmac_f32_e32 v29, 0xba000000, v25
	v_fmac_f32_e32 v27, 0xba000000, v25
	v_add_f32_e32 v24, v34, v24
	v_fmac_f32_e32 v28, 0xba000000, v25
	v_fmac_f32_e32 v26, 0xba000000, v25
	v_mul_f32_e32 v34, v27, v27
	v_mul_f32_e32 v60, v29, v29
	v_fmac_f32_e32 v34, v26, v26
	v_fmac_f32_e32 v60, v28, v28
	v_add_f32_e32 v34, v34, v60
	v_fmac_f32_e32 v21, 0xba000000, v25
	v_fmac_f32_e32 v23, 0xba000000, v25
	v_add_f32_e32 v24, v34, v24
	v_fmac_f32_e32 v20, 0xba000000, v25
	v_fmac_f32_e32 v22, 0xba000000, v25
	v_mul_f32_e32 v34, v23, v23
	v_mul_f32_e32 v60, v21, v21
	v_fmac_f32_e32 v34, v22, v22
	v_fmac_f32_e32 v60, v20, v20
	v_add_f32_e32 v34, v34, v60
	v_fmac_f32_e32 v19, 0xba000000, v25
	v_fmac_f32_e32 v17, 0xba000000, v25
	v_add_f32_e32 v24, v34, v24
	v_fmac_f32_e32 v18, 0xba000000, v25
	v_fmac_f32_e32 v16, 0xba000000, v25
	v_mul_f32_e32 v34, v17, v17
	v_mul_f32_e32 v60, v19, v19
	v_fmac_f32_e32 v34, v16, v16
	v_fmac_f32_e32 v60, v18, v18
	v_add_f32_e32 v34, v34, v60
	v_fmac_f32_e32 v13, 0xba000000, v25
	v_fmac_f32_e32 v15, 0xba000000, v25
	v_add_f32_e32 v24, v34, v24
	v_fmac_f32_e32 v12, 0xba000000, v25
	v_fmac_f32_e32 v14, 0xba000000, v25
	v_mul_f32_e32 v34, v15, v15
	v_mul_f32_e32 v60, v13, v13
	v_fmac_f32_e32 v34, v14, v14
	v_fmac_f32_e32 v60, v12, v12
	v_add_f32_e32 v34, v34, v60
	v_fmac_f32_e32 v9, 0xba000000, v25
	v_fmac_f32_e32 v11, 0xba000000, v25
	v_add_f32_e32 v24, v34, v24
	v_fmac_f32_e32 v8, 0xba000000, v25
	v_fmac_f32_e32 v10, 0xba000000, v25
	v_mul_f32_e32 v34, v11, v11
	v_mul_f32_e32 v60, v9, v9
	v_fmac_f32_e32 v34, v10, v10
	v_fmac_f32_e32 v60, v8, v8
	v_add_f32_e32 v34, v34, v60
	v_add_f32_e32 v24, v34, v24
	s_nop 1
	v_add_f32_dpp v24, v24, v24 quad_perm:[1,0,3,2] row_mask:0xf bank_mask:0xf bound_ctrl:1
	s_nop 1
	v_add_f32_dpp v24, v24, v24 quad_perm:[2,3,0,1] row_mask:0xf bank_mask:0xf bound_ctrl:1
	s_nop 1
	v_add_f32_dpp v24, v24, v24 row_half_mirror row_mask:0xf bank_mask:0xf bound_ctrl:1
	s_nop 1
	v_add_f32_dpp v24, v24, v24 row_mirror row_mask:0xf bank_mask:0xf bound_ctrl:1
	v_mov_b32_e32 v34, v24
	s_nop 1
	v_permlane16_swap_b32_e32 v24, v34
	v_add_f32_e32 v24, v24, v34
	v_mov_b32_e32 v34, v24
	s_nop 1
	v_permlane32_swap_b32_e32 v24, v34
	v_add_f32_e32 v24, v24, v34
	v_fmamk_f32 v24, v24, 0x3a000000, v135
	v_cmp_gt_f32_e32 vcc, s44, v24
	v_mul_f32_e32 v34, 0x4f800000, v24
	s_nop 0
	v_cndmask_b32_e32 v24, v24, v34, vcc
	v_sqrt_f32_e32 v34, v24
	s_nop 0
	v_add_u32_e32 v60, -1, v34
	v_fma_f32 v61, -v60, v34, v24
	v_cmp_ge_f32_e64 s[12:13], 0, v61
	v_add_u32_e32 v61, 1, v34
	s_nop 0
	v_cndmask_b32_e64 v60, v34, v60, s[12:13]
	v_fma_f32 v34, -v61, v34, v24
	v_cmp_lt_f32_e64 s[12:13], 0, v34
	s_nop 1
	v_cndmask_b32_e64 v34, v60, v61, s[12:13]
	v_mul_f32_e32 v60, 0x37800000, v34
	v_cndmask_b32_e32 v34, v34, v60, vcc
	v_cmp_class_f32_e32 vcc, v24, v136
	s_nop 1
	v_cndmask_b32_e32 v24, v34, v24, vcc
	v_div_scale_f32 v34, s[12:13], v24, v24, 1.0
	v_rcp_f32_e32 v60, v34
	s_nop 0
	v_fma_f32 v61, -v34, v60, 1.0
	v_fmac_f32_e32 v60, v61, v60
	v_div_scale_f32 v61, vcc, 1.0, v24, 1.0
	v_mul_f32_e32 v62, v61, v60
	v_fma_f32 v63, -v34, v62, v61
	v_fmac_f32_e32 v62, v63, v60
	v_fma_f32 v34, -v34, v62, v61
	v_div_fmas_f32 v34, v34, v60, v62
	v_div_fixup_f32 v24, v34, v24, 1.0
	v_pk_mul_f32 v[58:59], v[58:59], v[24:25] op_sel_hi:[1,0]
	v_pk_mul_f32 v[56:57], v[56:57], v[24:25] op_sel_hi:[1,0]
	v_pk_fma_f32 v[58:59], v[180:181], v[58:59], v[184:185]
	v_pk_fma_f32 v[56:57], v[182:183], v[56:57], v[186:187]
	v_cvt_pk_fp8_f32 v34, v58, v59
	v_pk_mul_f32 v[52:53], v[52:53], v[24:25] op_sel_hi:[1,0]
	v_pk_mul_f32 v[54:55], v[54:55], v[24:25] op_sel_hi:[1,0]
	v_pk_mul_f32 v[32:33], v[32:33], v[24:25] op_sel_hi:[1,0]
	v_cvt_pk_fp8_f32 v34, v56, v57 op_sel:[0,0,1]
	v_pk_mul_f32 v[30:31], v[30:31], v[24:25] op_sel_hi:[1,0]
	v_pk_mul_f32 v[26:27], v[26:27], v[24:25] op_sel_hi:[1,0]
	v_pk_mul_f32 v[28:29], v[28:29], v[24:25] op_sel_hi:[1,0]
	global_store_dword v[6:7], v34, off
	v_pk_mul_f32 v[22:23], v[22:23], v[24:25] op_sel_hi:[1,0]
	v_pk_mul_f32 v[20:21], v[20:21], v[24:25] op_sel_hi:[1,0]
	v_pk_mul_f32 v[16:17], v[16:17], v[24:25] op_sel_hi:[1,0]
	v_pk_fma_f32 v[52:53], v[188:189], v[52:53], v[192:193]
	v_pk_fma_f32 v[54:55], v[190:191], v[54:55], v[194:195]
	v_cvt_pk_fp8_f32 v34, v52, v53
	v_pk_mul_f32 v[18:19], v[18:19], v[24:25] op_sel_hi:[1,0]
	v_pk_mul_f32 v[14:15], v[14:15], v[24:25] op_sel_hi:[1,0]
	v_pk_mul_f32 v[12:13], v[12:13], v[24:25] op_sel_hi:[1,0]
	v_cvt_pk_fp8_f32 v34, v54, v55 op_sel:[0,0,1]
	v_pk_mul_f32 v[10:11], v[10:11], v[24:25] op_sel_hi:[1,0]
	v_pk_mul_f32 v[8:9], v[8:9], v[24:25] op_sel_hi:[1,0]
	global_store_dword v[6:7], v34, off offset:256
	v_pk_fma_f32 v[32:33], v[32:33], v[196:197], v[200:201]
	s_nop 0
	v_cvt_pk_fp8_f32 v34, v32, v33
	v_pk_fma_f32 v[30:31], v[30:31], v[198:199], v[202:203]
	s_nop 0
	v_cvt_pk_fp8_f32 v34, v30, v31 op_sel:[0,0,1]
	global_store_dword v[6:7], v34, off offset:512
	v_pk_fma_f32 v[26:27], v[26:27], v[204:205], v[208:209]
	v_cvt_pk_fp8_f32 v30, v26, v27
	v_pk_fma_f32 v[28:29], v[28:29], v[206:207], v[210:211]
	s_nop 0
	v_cvt_pk_fp8_f32 v30, v28, v29 op_sel:[0,0,1]
	global_store_dword v[6:7], v30, off offset:768
	v_pk_fma_f32 v[22:23], v[22:23], v[212:213], v[216:217]
	v_cvt_pk_fp8_f32 v26, v22, v23
	v_pk_fma_f32 v[20:21], v[20:21], v[214:215], v[218:219]
	s_nop 0
	v_cvt_pk_fp8_f32 v26, v20, v21 op_sel:[0,0,1]
	global_store_dword v[6:7], v26, off offset:1024
	v_pk_fma_f32 v[16:17], v[16:17], v[220:221], v[224:225]
	v_cvt_pk_fp8_f32 v20, v16, v17
	v_pk_fma_f32 v[18:19], v[18:19], v[222:223], v[226:227]
	s_nop 0
	v_cvt_pk_fp8_f32 v20, v18, v19 op_sel:[0,0,1]
	global_store_dword v[6:7], v20, off offset:1280
	v_pk_fma_f32 v[14:15], v[14:15], v[228:229], v[232:233]
	v_cvt_pk_fp8_f32 v16, v14, v15
	v_pk_fma_f32 v[12:13], v[12:13], v[230:231], v[234:235]
	s_nop 0
	v_cvt_pk_fp8_f32 v16, v12, v13 op_sel:[0,0,1]
	global_store_dword v[6:7], v16, off offset:1536
	v_pk_fma_f32 v[10:11], v[10:11], v[236:237], v[240:241]
	v_cvt_pk_fp8_f32 v12, v10, v11
	v_pk_fma_f32 v[8:9], v[8:9], v[238:239], v[242:243]
	s_nop 0
	v_cvt_pk_fp8_f32 v12, v8, v9 op_sel:[0,0,1]
	global_store_dword v[6:7], v12, off offset:1792
	s_and_saveexec_b64 s[12:13], s[8:9]
	s_cbranch_execz .LBB0_705
	s_add_u32 s68, s92, s14
	v_mul_f32_e32 v6, 0x3a000000, v25
	s_addc_u32 s69, s93, s15
	v_mov_b32_e32 v7, v24
	v_mov_b32_e32 v8, s37
	ds_write_b64 v8, v[6:7]
	global_store_dwordx2 v137, v[6:7], s[68:69] offset:8
	s_branch .LBB0_705
